# LN2: LayerNorm gain/bias loaded once per phase into 64 dead VGPRs instead of 16 loads + full vmcnt drains per row; next row's prefetch stays in flight through normalise/store; counted loop-top wait le
# speedup vs baseline: 1.0136x; 1.0036x over previous
.LBB0_1510:
	s_andn2_b64 vcc, exec, s[2:3]
	s_movk_i32 s33, 0x2000
	s_cbranch_vccnz .LBB0_105
	s_waitcnt vmcnt(0)
	v_mov_b32_e32 v1, v0
	v_readlane_b32 s2, v251, 29
	v_ashrrev_i32_e32 v52, 6, v1
	v_readlane_b32 s3, v251, 30
	v_add_u32_e32 v60, s2, v52
	v_cmp_gt_i32_e32 vcc, s33, v60
	s_and_saveexec_b64 s[6:7], vcc
	s_cbranch_execz .LBB0_1530
	v_ashrrev_i32_e32 v61, 31, v60
	v_readlane_b32 s2, v254, 23
	v_lshlrev_b64 v[4:5], 12, v[60:61]
	v_readlane_b32 s3, v254, 24
	v_lshlrev_b32_e32 v1, 4, v1
	v_lshl_add_u64 v[6:7], s[22:23], 0, v[4:5]
	v_lshl_add_u64 v[8:9], s[2:3], 0, v[4:5]
	v_readlane_b32 s2, v254, 27
	v_readlane_b32 s3, v254, 28
	v_and_b32_e32 v2, 0x3f0, v1
	v_lshl_add_u64 v[6:7], v[6:7], 0, v[2:3]
	v_lshl_add_u64 v[4:5], s[2:3], 0, v[4:5]
	v_lshl_add_u64 v[36:37], v[8:9], 0, v[2:3]
	v_lshl_add_u64 v[40:41], v[4:5], 0, v[2:3]
	global_load_dwordx4 v[24:27], v[6:7], off nt
	global_load_dwordx4 v[12:15], v[6:7], off offset:1024 nt
	global_load_dwordx4 v[28:31], v[36:37], off nt
	global_load_dwordx4 v[16:19], v[36:37], off offset:1024 nt
	global_load_dwordx4 v[32:35], v[40:41], off nt
	global_load_dwordx4 v[20:23], v[40:41], off offset:1024 nt
	global_load_dwordx4 v[8:11], v[6:7], off offset:2048 nt
	s_nop 0
	global_load_dwordx4 v[4:7], v[6:7], off offset:3072 nt
	s_nop 0
	global_load_dwordx4 v[44:47], v[36:37], off offset:2048 nt
	s_nop 0
	global_load_dwordx4 v[36:39], v[36:37], off offset:3072 nt
	s_nop 0
	global_load_dwordx4 v[48:51], v[40:41], off offset:2048 nt
	s_nop 0
	global_load_dwordx4 v[40:43], v[40:41], off offset:3072 nt
	s_lshl_b32 s2, s90, 12
	s_or_b32 s34, s2, 0x800
	v_readlane_b32 s8, v251, 0
	s_lshl_b64 s[2:3], s[34:35], 2
	v_readlane_b32 s10, v251, 2
	v_readlane_b32 s9, v251, 1
	v_readlane_b32 s11, v251, 3
	s_add_u32 s8, s10, s2
	v_readlane_b32 s12, v251, 4
	s_addc_u32 s9, s11, s3
	v_readlane_b32 s13, v251, 5
	s_add_u32 s10, s12, s2
	v_readlane_b32 s4, v251, 29
	s_addc_u32 s11, s13, s3
	v_ashrrev_i32_e32 v53, 31, v52
	v_readlane_b32 s5, v251, 30
	v_readlane_b32 s14, v251, 6
	v_readlane_b32 s15, v251, 7
	s_cmp_eq_u32 s90, 3
	v_lshl_add_u64 v[52:53], s[4:5], 0, v[52:53]
	s_cselect_b32 s3, s15, 0
	s_cselect_b32 s2, s14, 0
	v_lshlrev_b64 v[54:55], 12, v[52:53]
	v_readlane_b32 s4, v254, 45
	v_lshlrev_b64 v[52:53], 13, v[52:53]
	s_cmp_lg_u64 s[2:3], 0
	v_readlane_b32 s5, v254, 46
	v_lshl_add_u64 v[52:53], s[2:3], 0, v[52:53]
	s_mov_b64 s[2:3], 0x1000
	s_mov_b64 s[12:13], 0
	s_cselect_b64 s[14:15], -1, 0
	v_lshl_add_u64 v[62:63], s[4:5], 0, v[54:55]
	v_lshl_add_u64 v[64:65], v[52:53], 0, s[2:3]
	v_lshlrev_b32_e32 v224, 1, v2
	v_add_u32_e32 v225, 0x1000, v224
	s_nop 0
	global_load_dwordx4 v[152:155], v224, s[8:9] offset:16
	global_load_dwordx4 v[156:159], v224, s[8:9]
	global_load_dwordx4 v[160:163], v224, s[10:11] offset:16
	global_load_dwordx4 v[164:167], v224, s[10:11]
	global_load_dwordx4 v[168:171], v224, s[10:11] offset:2048
	global_load_dwordx4 v[172:175], v224, s[8:9] offset:2048
	global_load_dwordx4 v[176:179], v224, s[8:9] offset:2064
	global_load_dwordx4 v[180:183], v224, s[10:11] offset:2064
	global_load_dwordx4 v[184:187], v225, s[10:11]
	global_load_dwordx4 v[188:191], v225, s[8:9]
	global_load_dwordx4 v[192:195], v225, s[8:9] offset:16
	global_load_dwordx4 v[196:199], v225, s[10:11] offset:16
	global_load_dwordx4 v[208:211], v225, s[10:11] offset:2048
	global_load_dwordx4 v[212:215], v225, s[8:9] offset:2048
	global_load_dwordx4 v[216:219], v225, s[8:9] offset:2064
	global_load_dwordx4 v[220:223], v225, s[10:11] offset:2064
	s_waitcnt vmcnt(0)
	s_branch .LBB0_1515

.LBB0_1515:
	s_waitcnt vmcnt(4)
	v_lshlrev_b32_e32 v52, 16, v28
	v_and_b32_e32 v53, 0xffff0000, v28
	v_lshlrev_b32_e32 v28, 16, v29
	v_and_b32_e32 v29, 0xffff0000, v29
	v_lshlrev_b32_e32 v56, 16, v32
	v_and_b32_e32 v57, 0xffff0000, v32
	v_lshlrev_b32_e32 v32, 16, v33
	v_and_b32_e32 v33, 0xffff0000, v33
	v_lshlrev_b32_e32 v54, 16, v24
	v_and_b32_e32 v55, 0xffff0000, v24
	v_lshlrev_b32_e32 v24, 16, v25
	v_and_b32_e32 v25, 0xffff0000, v25
	v_pk_add_f32 v[28:29], v[28:29], v[32:33]
	v_pk_add_f32 v[56:57], v[52:53], v[56:57]
	v_pk_fma_f32 v[52:53], v[24:25], s[28:29], v[28:29] op_sel_hi:[1,0,1]
	v_lshlrev_b32_e32 v28, 16, v30
	v_and_b32_e32 v29, 0xffff0000, v30
	v_lshlrev_b32_e32 v32, 16, v34
	v_and_b32_e32 v33, 0xffff0000, v34
	v_lshlrev_b32_e32 v24, 16, v26
	v_and_b32_e32 v25, 0xffff0000, v26
	v_lshlrev_b32_e32 v30, 16, v31
	v_and_b32_e32 v31, 0xffff0000, v31
	v_lshlrev_b32_e32 v34, 16, v35
	v_and_b32_e32 v35, 0xffff0000, v35
	v_pk_add_f32 v[28:29], v[28:29], v[32:33]
	v_pk_fma_f32 v[54:55], v[54:55], s[28:29], v[56:57] op_sel_hi:[1,0,1]
	v_lshlrev_b32_e32 v26, 16, v27
	v_and_b32_e32 v27, 0xffff0000, v27
	v_pk_add_f32 v[30:31], v[30:31], v[34:35]
	v_pk_fma_f32 v[58:59], v[24:25], s[28:29], v[28:29] op_sel_hi:[1,0,1]
	v_pk_fma_f32 v[56:57], v[26:27], s[28:29], v[30:31] op_sel_hi:[1,0,1]
	v_mov_b32_e32 v24, v58
	v_mov_b32_e32 v25, v54
	v_mov_b32_e32 v26, v59
	v_mov_b32_e32 v27, v55
	v_pk_add_f32 v[24:25], v[24:25], v[26:27]
	v_mov_b32_e32 v26, v56
	v_mov_b32_e32 v27, v52
	v_mov_b32_e32 v28, v57
	v_mov_b32_e32 v29, v53
	v_pk_add_f32 v[26:27], v[26:27], v[28:29]
	v_lshlrev_b32_e32 v28, 16, v16
	v_and_b32_e32 v29, 0xffff0000, v16
	v_lshlrev_b32_e32 v16, 16, v17
	v_and_b32_e32 v17, 0xffff0000, v17
	v_lshlrev_b32_e32 v30, 16, v20
	v_and_b32_e32 v31, 0xffff0000, v20
	v_lshlrev_b32_e32 v20, 16, v21
	v_and_b32_e32 v21, 0xffff0000, v21
	v_pk_add_f32 v[24:25], v[24:25], v[26:27]
	v_lshlrev_b32_e32 v26, 16, v12
	v_and_b32_e32 v27, 0xffff0000, v12
	v_lshlrev_b32_e32 v12, 16, v13
	v_and_b32_e32 v13, 0xffff0000, v13
	v_pk_add_f32 v[16:17], v[16:17], v[20:21]
	v_pk_add_f32 v[28:29], v[28:29], v[30:31]
	v_pk_fma_f32 v[74:75], v[12:13], s[28:29], v[16:17] op_sel_hi:[1,0,1]
	v_lshlrev_b32_e32 v16, 16, v18
	v_and_b32_e32 v17, 0xffff0000, v18
	v_lshlrev_b32_e32 v18, 16, v19
	v_and_b32_e32 v19, 0xffff0000, v19
	v_lshlrev_b32_e32 v20, 16, v22
	v_and_b32_e32 v21, 0xffff0000, v22
	v_lshlrev_b32_e32 v22, 16, v23
	v_and_b32_e32 v23, 0xffff0000, v23
	v_pk_fma_f32 v[78:79], v[26:27], s[28:29], v[28:29] op_sel_hi:[1,0,1]
	v_lshlrev_b32_e32 v12, 16, v14
	v_and_b32_e32 v13, 0xffff0000, v14
	v_lshlrev_b32_e32 v14, 16, v15
	v_and_b32_e32 v15, 0xffff0000, v15
	v_pk_add_f32 v[16:17], v[16:17], v[20:21]
	v_pk_add_f32 v[18:19], v[18:19], v[22:23]
	v_pk_fma_f32 v[92:93], v[12:13], s[28:29], v[16:17] op_sel_hi:[1,0,1]
	v_pk_fma_f32 v[90:91], v[14:15], s[28:29], v[18:19] op_sel_hi:[1,0,1]
	v_pk_mov_b32 v[12:13], v[78:79], v[74:75] op_sel:[1,0]
	v_mov_b32_e32 v14, v78
	v_mov_b32_e32 v15, v75
	v_pk_add_f32 v[12:13], v[12:13], v[14:15]
	v_pk_mov_b32 v[14:15], v[92:93], v[90:91] op_sel:[1,0]
	v_mov_b32_e32 v16, v92
	v_mov_b32_e32 v17, v91
	v_lshlrev_b32_e32 v18, 16, v44
	v_and_b32_e32 v19, 0xffff0000, v44
	v_lshlrev_b32_e32 v22, 16, v48
	v_and_b32_e32 v23, 0xffff0000, v48
	v_pk_add_f32 v[14:15], v[14:15], v[16:17]
	v_lshlrev_b32_e32 v16, 16, v8
	v_and_b32_e32 v17, 0xffff0000, v8
	v_lshlrev_b32_e32 v20, 16, v45
	v_and_b32_e32 v21, 0xffff0000, v45
	v_lshlrev_b32_e32 v26, 16, v49
	v_and_b32_e32 v27, 0xffff0000, v49
	v_pk_add_f32 v[18:19], v[18:19], v[22:23]
	v_lshlrev_b32_e32 v8, 16, v9
	v_and_b32_e32 v9, 0xffff0000, v9
	v_pk_add_f32 v[20:21], v[20:21], v[26:27]
	v_pk_fma_f32 v[82:83], v[16:17], s[28:29], v[18:19] op_sel_hi:[1,0,1]
	v_lshlrev_b32_e32 v18, 16, v47
	v_and_b32_e32 v19, 0xffff0000, v47
	v_lshlrev_b32_e32 v22, 16, v51
	v_and_b32_e32 v23, 0xffff0000, v51
	v_pk_fma_f32 v[68:69], v[8:9], s[28:29], v[20:21] op_sel_hi:[1,0,1]
	v_lshlrev_b32_e32 v16, 16, v46
	v_and_b32_e32 v17, 0xffff0000, v46
	v_lshlrev_b32_e32 v20, 16, v50
	v_and_b32_e32 v21, 0xffff0000, v50
	v_pk_add_f32 v[18:19], v[18:19], v[22:23]
	v_lshlrev_b32_e32 v22, 16, v36
	v_and_b32_e32 v23, 0xffff0000, v36
	v_lshlrev_b32_e32 v26, 16, v37
	v_and_b32_e32 v27, 0xffff0000, v37
	v_lshlrev_b32_e32 v28, 16, v40
	v_and_b32_e32 v29, 0xffff0000, v40
	v_lshlrev_b32_e32 v30, 16, v41
	v_and_b32_e32 v31, 0xffff0000, v41
	v_pk_add_f32 v[16:17], v[16:17], v[20:21]
	v_lshlrev_b32_e32 v20, 16, v4
	v_and_b32_e32 v21, 0xffff0000, v4
	v_lshlrev_b32_e32 v4, 16, v5
	v_and_b32_e32 v5, 0xffff0000, v5
	v_pk_add_f32 v[22:23], v[22:23], v[28:29]
	v_pk_add_f32 v[26:27], v[26:27], v[30:31]
	v_mov_b32_e32 v2, v60
	v_pk_fma_f32 v[66:67], v[4:5], s[28:29], v[26:27] op_sel_hi:[1,0,1]
	v_pk_fma_f32 v[72:73], v[20:21], s[28:29], v[22:23] op_sel_hi:[1,0,1]
	v_lshlrev_b32_e32 v20, 16, v38
	v_and_b32_e32 v21, 0xffff0000, v38
	v_lshlrev_b32_e32 v26, 16, v42
	v_and_b32_e32 v27, 0xffff0000, v42
	v_add_u32_e32 v60, s88, v2
	v_lshlrev_b32_e32 v4, 16, v6
	v_and_b32_e32 v5, 0xffff0000, v6
	v_pk_add_f32 v[20:21], v[20:21], v[26:27]
	v_cmp_gt_i32_e32 vcc, s33, v60
	v_pk_fma_f32 v[76:77], v[4:5], s[28:29], v[20:21] op_sel_hi:[1,0,1]
	v_readlane_b32 s2, v254, 23
	v_cndmask_b32_e32 v4, v2, v60, vcc
	v_ashrrev_i32_e32 v5, 31, v4
	v_mov_b32_e32 v1, v0
	v_lshlrev_b64 v[4:5], 12, v[4:5]
	v_readlane_b32 s3, v254, 24
	v_lshlrev_b32_e32 v22, 16, v39
	v_and_b32_e32 v23, 0xffff0000, v39
	v_lshlrev_b32_e32 v28, 16, v43
	v_and_b32_e32 v29, 0xffff0000, v43
	v_lshlrev_b32_e32 v2, 3, v1
	v_lshl_add_u64 v[20:21], s[2:3], 0, v[4:5]
	v_readlane_b32 s2, v254, 27
	v_lshlrev_b32_e32 v8, 16, v10
	v_and_b32_e32 v9, 0xffff0000, v10
	v_lshlrev_b32_e32 v10, 16, v11
	v_and_b32_e32 v11, 0xffff0000, v11
	v_lshlrev_b32_e32 v6, 16, v7
	v_and_b32_e32 v7, 0xffff0000, v7
	v_pk_add_f32 v[22:23], v[22:23], v[28:29]
	v_and_b32_e32 v61, 0x1f8, v2
	v_readlane_b32 s3, v254, 28
	v_pk_add_f32 v[24:25], v[24:25], v[24:25] op_sel_hi:[0,1]
	v_pk_add_f32 v[12:13], v[12:13], v[12:13] op_sel_hi:[0,1]
	v_pk_add_f32 v[14:15], v[14:15], v[14:15] op_sel_hi:[0,1]
	v_pk_fma_f32 v[80:81], v[10:11], s[28:29], v[18:19] op_sel_hi:[1,0,1]
	v_pk_fma_f32 v[88:89], v[8:9], s[28:29], v[16:17] op_sel_hi:[1,0,1]
	v_pk_fma_f32 v[70:71], v[6:7], s[28:29], v[22:23] op_sel_hi:[1,0,1]
	v_lshl_add_u64 v[6:7], s[22:23], 0, v[4:5]
	v_lshl_add_u64 v[4:5], s[2:3], 0, v[4:5]
	v_lshlrev_b32_e32 v2, 1, v61
	v_add_f32_e32 v9, v82, v83
	v_add_f32_e32 v11, v68, v69
	v_add_f32_e32 v17, v88, v89
	v_add_f32_e32 v19, v80, v81
	v_lshl_add_u64 v[6:7], v[6:7], 0, v[2:3]
	v_lshl_add_u64 v[36:37], v[20:21], 0, v[2:3]
	v_lshl_add_u64 v[40:41], v[4:5], 0, v[2:3]
	v_mov_b32_e32 v14, v72
	v_mov_b32_e32 v12, v73
	v_mov_b32_e32 v16, v76
	v_mov_b32_e32 v18, v77
	v_mov_b32_e32 v8, v70
	v_mov_b32_e32 v10, v71
	v_mov_b32_e32 v24, v66
	v_mov_b32_e32 v2, v67
	v_pk_add_f32 v[4:5], v[14:15], v[12:13]
	v_pk_add_f32 v[12:13], v[16:17], v[18:19]
	v_pk_add_f32 v[8:9], v[8:9], v[10:11]
	v_pk_add_f32 v[10:11], v[24:25], v[2:3]
	v_pk_add_f32 v[8:9], v[12:13], v[8:9]
	v_pk_add_f32 v[4:5], v[4:5], v[10:11]
	global_load_dwordx4 v[24:27], v[6:7], off nt
	global_load_dwordx4 v[12:15], v[6:7], off offset:1024 nt
	global_load_dwordx4 v[28:31], v[36:37], off nt
	global_load_dwordx4 v[16:19], v[36:37], off offset:1024 nt
	v_pk_add_f32 v[4:5], v[8:9], v[4:5]
	s_mov_b32 s2, 0xf800000
	v_add_f32_e32 v2, v4, v5
	v_and_b32_e32 v4, 64, v229
	v_add_u32_e32 v4, 64, v4
	v_xor_b32_e32 v5, 1, v229
	v_cmp_lt_i32_e32 vcc, v5, v4
	v_and_b32_e32 v1, 63, v1
	s_nop 0
	v_cndmask_b32_e32 v5, v229, v5, vcc
	v_lshlrev_b32_e32 v48, 2, v5
	ds_bpermute_b32 v5, v48, v2
	s_waitcnt lgkmcnt(0)
	v_add_f32_e32 v2, v2, v5
	v_xor_b32_e32 v5, 2, v229
	v_cmp_lt_i32_e32 vcc, v5, v4
	s_nop 1
	v_cndmask_b32_e32 v5, v229, v5, vcc
	v_lshlrev_b32_e32 v94, 2, v5
	ds_bpermute_b32 v5, v94, v2
	s_waitcnt lgkmcnt(0)
	v_add_f32_e32 v2, v2, v5
	v_xor_b32_e32 v5, 4, v229
	v_cmp_lt_i32_e32 vcc, v5, v4
	s_nop 1
	v_cndmask_b32_e32 v5, v229, v5, vcc
	v_lshlrev_b32_e32 v95, 2, v5
	ds_bpermute_b32 v5, v95, v2
	s_waitcnt lgkmcnt(0)
	v_add_f32_e32 v2, v2, v5
	v_xor_b32_e32 v5, 8, v229
	v_cmp_lt_i32_e32 vcc, v5, v4
	s_nop 1
	v_cndmask_b32_e32 v5, v229, v5, vcc
	v_lshlrev_b32_e32 v96, 2, v5
	ds_bpermute_b32 v5, v96, v2
	s_waitcnt lgkmcnt(0)
	v_add_f32_e32 v2, v2, v5
	v_xor_b32_e32 v5, 16, v229
	v_cmp_lt_i32_e32 vcc, v5, v4
	s_nop 1
	v_cndmask_b32_e32 v5, v229, v5, vcc
	v_lshlrev_b32_e32 v97, 2, v5
	ds_bpermute_b32 v5, v97, v2
	s_waitcnt lgkmcnt(0)
	v_add_f32_e32 v2, v2, v5
	v_xor_b32_e32 v5, 32, v229
	v_cmp_lt_i32_e32 vcc, v5, v4
	s_nop 1
	v_cndmask_b32_e32 v4, v229, v5, vcc
	v_lshlrev_b32_e32 v114, 2, v4
	ds_bpermute_b32 v38, v114, v2
	global_load_dwordx4 v[32:35], v[40:41], off nt
	global_load_dwordx4 v[20:23], v[40:41], off offset:1024 nt
	global_load_dwordx4 v[8:11], v[6:7], off offset:2048 nt
	s_nop 0
	global_load_dwordx4 v[4:7], v[6:7], off offset:3072 nt
	s_waitcnt lgkmcnt(0)
	v_add_f32_e32 v49, v2, v38
	v_fmamk_f32 v55, v49, 0xba000000, v55
	v_fmamk_f32 v59, v49, 0xba000000, v59
	v_fmamk_f32 v53, v49, 0xba000000, v53
	v_fmac_f32_e32 v54, 0xba000000, v49
	v_fmamk_f32 v57, v49, 0xba000000, v57
	v_fmac_f32_e32 v58, 0xba000000, v49
	v_mov_b32_e32 v42, v55
	v_mov_b32_e32 v43, v59
	v_fmac_f32_e32 v52, 0xba000000, v49
	v_fmac_f32_e32 v56, 0xba000000, v49
	v_mov_b32_e32 v38, v54
	v_mov_b32_e32 v39, v58
	v_pk_mul_f32 v[42:43], v[42:43], v[42:43]
	v_mov_b32_e32 v44, v53
	v_mov_b32_e32 v45, v57
	v_pk_fma_f32 v[38:39], v[38:39], v[38:39], v[42:43]
	v_mov_b32_e32 v42, v52
	v_mov_b32_e32 v43, v56
	v_pk_mul_f32 v[44:45], v[44:45], v[44:45]
	v_fmamk_f32 v75, v49, 0xba000000, v75
	v_pk_fma_f32 v[42:43], v[42:43], v[42:43], v[44:45]
	v_fmac_f32_e32 v74, 0xba000000, v49
	v_fmamk_f32 v79, v49, 0xba000000, v79
	v_fmac_f32_e32 v78, 0xba000000, v49
	v_pk_add_f32 v[38:39], v[38:39], v[42:43]
	v_pk_mul_f32 v[42:43], v[74:75], v[74:75]
	v_pk_mul_f32 v[44:45], v[78:79], v[78:79]
	v_fmac_f32_e32 v92, 0xba000000, v49
	v_pk_mov_b32 v[46:47], v[44:45], v[42:43] op_sel:[1,0]
	v_mov_b32_e32 v45, v43
	v_fmac_f32_e32 v90, 0xba000000, v49
	v_fmamk_f32 v93, v49, 0xba000000, v93
	v_mul_f32_e32 v2, v92, v92
	v_pk_add_f32 v[42:43], v[46:47], v[44:45]
	v_fmamk_f32 v91, v49, 0xba000000, v91
	v_pk_fma_f32 v[44:45], v[92:93], v[92:93], v[2:3] op_sel_hi:[1,1,0]
	v_mul_f32_e32 v2, v90, v90
	v_pk_add_f32 v[38:39], v[38:39], v[38:39] op_sel_hi:[0,1]
	v_pk_add_f32 v[42:43], v[42:43], v[42:43] op_sel_hi:[0,1]
	v_pk_fma_f32 v[46:47], v[90:91], v[90:91], v[2:3] op_sel_hi:[1,1,0]
	v_fmamk_f32 v69, v49, 0xba000000, v69
	v_fmac_f32_e32 v68, 0xba000000, v49
	v_fmamk_f32 v83, v49, 0xba000000, v83
	v_fmac_f32_e32 v82, 0xba000000, v49
	v_mul_f32_e32 v44, v82, v82
	v_mul_f32_e32 v46, v83, v83
	v_mul_f32_e32 v42, v68, v68
	v_mul_f32_e32 v38, v69, v69
	v_pk_add_f32 v[44:45], v[44:45], v[46:47]
	v_pk_add_f32 v[38:39], v[42:43], v[38:39]
	v_fmamk_f32 v81, v49, 0xba000000, v81
	v_fmac_f32_e32 v80, 0xba000000, v49
	v_fmamk_f32 v89, v49, 0xba000000, v89
	v_fmac_f32_e32 v88, 0xba000000, v49
	v_pk_add_f32 v[38:39], v[44:45], v[38:39]
	v_pk_mul_f32 v[42:43], v[80:81], v[80:81]
	v_pk_mul_f32 v[44:45], v[88:89], v[88:89]
	v_fmac_f32_e32 v72, 0xba000000, v49
	v_pk_mov_b32 v[46:47], v[44:45], v[42:43] op_sel:[1,0]
	v_mov_b32_e32 v45, v43
	v_fmac_f32_e32 v66, 0xba000000, v49
	v_fmamk_f32 v73, v49, 0xba000000, v73
	v_mul_f32_e32 v2, v72, v72
	v_pk_add_f32 v[42:43], v[46:47], v[44:45]
	v_fmamk_f32 v67, v49, 0xba000000, v67
	v_pk_fma_f32 v[44:45], v[72:73], v[72:73], v[2:3] op_sel_hi:[1,1,0]
	v_mul_f32_e32 v2, v66, v66
	v_pk_add_f32 v[38:39], v[38:39], v[38:39] op_sel_hi:[0,1]
	v_pk_add_f32 v[42:43], v[42:43], v[42:43] op_sel_hi:[0,1]
	v_pk_fma_f32 v[46:47], v[66:67], v[66:67], v[2:3] op_sel_hi:[1,1,0]
	v_fmamk_f32 v71, v49, 0xba000000, v71
	v_fmac_f32_e32 v70, 0xba000000, v49
	v_fmamk_f32 v77, v49, 0xba000000, v77
	v_fmac_f32_e32 v76, 0xba000000, v49
	v_mul_f32_e32 v44, v76, v76
	v_mul_f32_e32 v46, v77, v77
	v_mul_f32_e32 v42, v70, v70
	v_mul_f32_e32 v38, v71, v71
	v_pk_add_f32 v[44:45], v[44:45], v[46:47]
	v_pk_add_f32 v[38:39], v[42:43], v[38:39]
	v_lshlrev_b32_e32 v2, 2, v61
	v_pk_add_f32 v[38:39], v[44:45], v[38:39]
	v_add_f32_e32 v115, v38, v39
	ds_bpermute_b32 v116, v48, v115
	global_load_dwordx4 v[44:47], v[36:37], off offset:2048 nt
	s_nop 0
	global_load_dwordx4 v[36:39], v[36:37], off offset:3072 nt
	s_nop 0
	global_load_dwordx4 v[48:51], v[40:41], off offset:2048 nt
	s_nop 0
	global_load_dwordx4 v[40:43], v[40:41], off offset:3072 nt
	s_waitcnt lgkmcnt(0)
	v_add_f32_e32 v115, v115, v116
	ds_bpermute_b32 v94, v94, v115
	s_waitcnt lgkmcnt(0)
	v_add_f32_e32 v94, v115, v94
	ds_bpermute_b32 v95, v95, v94
	s_waitcnt lgkmcnt(0)
	v_add_f32_e32 v94, v94, v95
	ds_bpermute_b32 v95, v96, v94
	s_waitcnt lgkmcnt(0)
	v_add_f32_e32 v94, v94, v95
	ds_bpermute_b32 v95, v97, v94
	s_waitcnt lgkmcnt(0)
	v_add_f32_e32 v94, v94, v95
	ds_bpermute_b32 v95, v114, v94
	s_waitcnt lgkmcnt(0)
	v_add_f32_e32 v94, v94, v95
	v_fmamk_f32 v94, v94, 0x3a000000, v232
	v_mul_f32_e32 v95, 0x4f800000, v94
	v_cmp_gt_f32_e32 vcc, s2, v94
	s_nop 1
	v_cndmask_b32_e32 v94, v94, v95, vcc
	v_sqrt_f32_e32 v95, v94
	s_nop 0
	v_add_u32_e32 v96, -1, v95
	v_fma_f32 v97, -v96, v95, v94
	v_cmp_ge_f32_e64 s[2:3], 0, v97
	v_add_u32_e32 v97, 1, v95
	s_nop 0
	v_cndmask_b32_e64 v96, v95, v96, s[2:3]
	v_fma_f32 v95, -v97, v95, v94
	v_cmp_lt_f32_e64 s[2:3], 0, v95
	s_nop 1
	v_cndmask_b32_e64 v95, v96, v97, s[2:3]
	v_mul_f32_e32 v96, 0x37800000, v95
	v_cndmask_b32_e32 v95, v95, v96, vcc
	v_cmp_class_f32_e32 vcc, v94, v231
	s_nop 1
	v_cndmask_b32_e32 v94, v95, v94, vcc
	v_div_scale_f32 v95, s[2:3], v94, v94, 1.0
	v_rcp_f32_e32 v96, v95
	s_movk_i32 s2, 0x1fff
	v_cmp_lt_i32_e64 s[2:3], s2, v60
	v_fma_f32 v97, -v95, v96, 1.0
	v_fmac_f32_e32 v96, v97, v96
	v_div_scale_f32 v97, vcc, 1.0, v94, 1.0
	v_mul_f32_e32 v114, v97, v96
	v_fma_f32 v115, -v95, v114, v97
	v_fmac_f32_e32 v114, v115, v96
	v_fma_f32 v95, -v95, v114, v97
	v_div_fmas_f32 v95, v95, v96, v114
	v_div_fixup_f32 v96, v95, v94, 1.0
	v_pk_mul_f32 v[94:95], v[54:55], v[96:97] op_sel_hi:[1,0]
	v_pk_mul_f32 v[52:53], v[52:53], v[96:97] op_sel_hi:[1,0]
	v_pk_mul_f32 v[56:57], v[56:57], v[96:97] op_sel_hi:[1,0]
	v_pk_fma_f32 v[54:55], v[158:159], v[52:53], v[166:167]
	v_pk_fma_f32 v[52:53], v[156:157], v[94:95], v[164:165]
	v_pk_mul_f32 v[94:95], v[58:59], v[96:97] op_sel_hi:[1,0]
	v_pk_fma_f32 v[58:59], v[154:155], v[56:57], v[162:163]
	v_pk_fma_f32 v[56:57], v[152:153], v[94:95], v[160:161]
	v_cndmask_b32_e64 v94, 0, 1, s[14:15]
	v_cmp_ne_u32_e64 s[4:5], 1, v94
	s_andn2_b64 vcc, exec, s[14:15]
	v_lshlrev_b32_e32 v98, 5, v1
	s_cbranch_vccnz .LBB0_1526
	v_mov_b32_e32 v99, v3
	v_lshl_add_u64 v[94:95], v[64:65], 0, v[98:99]
	global_store_dwordx4 v[94:95], v[52:55], off offset:-4096
	global_store_dwordx4 v[94:95], v[56:59], off offset:-4080
	v_lshlrev_b32_e32 v94, 4, v1
	s_cbranch_execnz .LBB0_1518

.LBB0_1518:
	v_mov_b32_e32 v97, v96
	v_mov_b32_e32 v108, v96
	v_mov_b32_e32 v109, v96
	v_pk_mul_f32 v[74:75], v[74:75], v[108:109]
	v_pk_mul_f32 v[78:79], v[78:79], v[96:97]
	v_pk_mul_f32 v[90:91], v[90:91], v[108:109]
	v_pk_mul_f32 v[92:93], v[92:93], v[96:97]
	s_and_b64 vcc, exec, s[4:5]
	v_pk_fma_f32 v[58:59], v[74:75], v[174:175], v[170:171]
	v_pk_fma_f32 v[56:57], v[78:79], v[172:173], v[168:169]
	v_pk_fma_f32 v[54:55], v[90:91], v[178:179], v[182:183]
	v_pk_fma_f32 v[52:53], v[92:93], v[176:177], v[180:181]
	s_cbranch_vccnz .LBB0_1527
	v_mov_b32_e32 v99, v3
	v_lshl_add_u64 v[74:75], v[64:65], 0, v[98:99]
	global_store_dwordx4 v[74:75], v[56:59], off offset:-2048
	global_store_dwordx4 v[74:75], v[52:55], off offset:-2032
	s_cbranch_execnz .LBB0_1521

.LBB0_1521:
	v_lshl_or_b32 v1, v61, 2, v237
	v_mov_b32_e32 v74, v96
	v_mov_b32_e32 v75, v96
	v_pk_mul_f32 v[78:79], v[82:83], v[96:97]
	v_pk_mul_f32 v[82:83], v[88:89], v[96:97]
	v_pk_mul_f32 v[68:69], v[68:69], v[74:75]
	v_pk_mul_f32 v[74:75], v[80:81], v[74:75]
	s_and_b64 vcc, exec, s[4:5]
	v_pk_fma_f32 v[58:59], v[68:69], v[190:191], v[186:187]
	v_pk_fma_f32 v[56:57], v[78:79], v[188:189], v[184:185]
	v_pk_fma_f32 v[54:55], v[74:75], v[194:195], v[198:199]
	v_pk_fma_f32 v[52:53], v[82:83], v[192:193], v[196:197]
	s_cbranch_vccnz .LBB0_1528
	v_mov_b32_e32 v99, v3
	v_lshl_add_u64 v[68:69], v[64:65], 0, v[98:99]
	global_store_dwordx4 v[68:69], v[56:59], off
	global_store_dwordx4 v[68:69], v[52:55], off offset:16
	s_cbranch_execnz .LBB0_1524

.LBB0_1524:
	v_lshl_or_b32 v1, v61, 2, v238
	v_mov_b32_e32 v68, v96
	v_mov_b32_e32 v69, v96
	v_pk_mul_f32 v[72:73], v[72:73], v[96:97]
	v_pk_mul_f32 v[74:75], v[76:77], v[96:97]
	v_pk_mul_f32 v[66:67], v[66:67], v[68:69]
	v_pk_mul_f32 v[68:69], v[70:71], v[68:69]
	s_and_b64 vcc, exec, s[4:5]
	v_pk_fma_f32 v[58:59], v[66:67], v[214:215], v[210:211]
	v_pk_fma_f32 v[56:57], v[72:73], v[212:213], v[208:209]
	v_pk_fma_f32 v[54:55], v[68:69], v[218:219], v[222:223]
	v_pk_fma_f32 v[52:53], v[74:75], v[216:217], v[220:221]
	s_cbranch_vccnz .LBB0_1529
	v_mov_b32_e32 v99, v3
	v_lshl_add_u64 v[66:67], v[64:65], 0, v[98:99]
	global_store_dwordx4 v[66:67], v[56:59], off offset:2048
	global_store_dwordx4 v[66:67], v[52:55], off offset:2064
	s_cbranch_execnz .LBB0_1514
	s_branch .LBB0_1513
